# v39
# speedup vs baseline: 1.0058x; 1.0058x over previous
.LBB0_34:
	s_or_b64 exec, exec, s[10:11]
	ds_read_b128 v[18:21], v72
	s_waitcnt vmcnt(3)
	v_cvt_pk_f16_f32 v14, v14, v15
	v_cvt_pk_f16_f32 v15, v16, v17
	v_cvt_pk_f16_f32 v16, v10, v11
	ds_read_b128 v[22:25], v71 offset:41984
	v_cvt_pk_f16_f32 v17, v12, v13
	ds_read_b128 v[10:13], v72 offset:1024
	ds_read_b128 v[26:29], v71 offset:42048
	s_waitcnt vmcnt(1)
	v_cvt_pk_f16_f32 v0, v6, v7
	v_cvt_pk_f16_f32 v1, v8, v9
	v_cvt_pk_f16_f32 v2, v2, v3
	v_cvt_pk_f16_f32 v3, v4, v5
	s_waitcnt lgkmcnt(2)
	v_mfma_f32_16x16x32_f16 v[30:33], v[18:21], v[14:17], v[22:25]
	s_add_i32 s10, s20, s12
	v_mfma_f32_16x16x32_f16 v[18:21], v[18:21], v[0:3], v[22:25]
	ds_read_b128 v[4:7], v72 offset:2048
	s_nop 1
	ds_read_b128 v[22:25], v71 offset:42112
	s_waitcnt lgkmcnt(2)
	v_mfma_f32_16x16x32_f16 v[34:37], v[10:13], v[14:17], v[26:29]
	v_exp_f32_e32 v78, v30
	v_exp_f32_e32 v79, v31
	v_exp_f32_e32 v20, v20
	v_mfma_f32_16x16x32_f16 v[8:11], v[10:13], v[0:3], v[26:29]
	ds_read_b128 v[44:47], v71 offset:42176
	s_nop 2
	v_exp_f32_e64 v80, v34 clamp
	v_exp_f32_e64 v81, v35 clamp
	ds_read_b128 v[26:29], v72 offset:3072
	s_waitcnt lgkmcnt(2)
	v_mfma_f32_16x16x32_f16 v[48:51], v[4:7], v[14:17], v[22:25]
	v_exp_f32_e64 v82, v36 clamp
	v_exp_f32_e64 v83, v37 clamp
	v_exp_f32_e32 v21, v21
	v_mfma_f32_16x16x32_f16 v[22:25], v[4:7], v[0:3], v[22:25]
	ds_read_b128 v[52:55], v72 offset:4096
	ds_read_b128 v[56:59], v71 offset:42240
	s_nop 1
	v_exp_f32_e32 v4, v48
	s_waitcnt lgkmcnt(2)
	v_mfma_f32_16x16x32_f16 v[60:63], v[26:29], v[14:17], v[44:47]
	v_exp_f32_e32 v5, v49
	v_exp_f32_e32 v48, v32
	v_exp_f32_e32 v49, v33
	v_mfma_f32_16x16x32_f16 v[26:29], v[26:29], v[0:3], v[44:47]
	ds_read_b128 v[64:67], v71 offset:42304
	v_exp_f32_e32 v6, v50
	v_exp_f32_e32 v7, v51
	ds_read_b128 v[44:47], v72 offset:5120
	s_waitcnt lgkmcnt(2)
	v_mfma_f32_16x16x32_f16 v[74:77], v[52:55], v[14:17], v[56:59]
	v_exp_f32_e32 v50, v18
	v_exp_f32_e32 v51, v19
	v_exp_f32_e32 v26, v26
	v_mfma_f32_16x16x32_f16 v[30:33], v[52:55], v[0:3], v[56:59]
	v_exp_f32_e64 v52, v8 clamp
	v_exp_f32_e64 v53, v9 clamp
	v_exp_f32_e32 v8, v22
	s_waitcnt lgkmcnt(0)
	v_mfma_f32_16x16x32_f16 v[34:37], v[44:47], v[14:17], v[64:67]
	v_exp_f32_e32 v9, v23
	v_exp_f32_e64 v22, v10 clamp
	v_exp_f32_e64 v23, v11 clamp
	v_mfma_f32_16x16x32_f16 v[44:47], v[44:47], v[0:3], v[64:67]
	v_exp_f32_e32 v10, v24
	v_exp_f32_e32 v11, v25
	s_nop 1
	v_exp_f32_e32 v12, v34
	v_exp_f32_e32 v13, v35
	v_exp_f32_e32 v18, v36
	v_exp_f32_e32 v24, v60
	v_exp_f32_e32 v25, v61
	v_exp_f32_e64 v54, v74 clamp
	v_exp_f32_e64 v55, v75 clamp
	v_exp_f32_e32 v34, v62
	v_exp_f32_e32 v35, v63
	v_exp_f32_e64 v56, v76 clamp
	v_exp_f32_e64 v57, v77 clamp
	v_exp_f32_e32 v19, v37
	v_exp_f32_e32 v27, v27
	v_exp_f32_e64 v30, v30 clamp
	v_exp_f32_e64 v31, v31 clamp
	v_exp_f32_e32 v36, v44
	v_exp_f32_e32 v37, v45
	v_exp_f32_e32 v28, v28
	v_exp_f32_e32 v29, v29
	v_exp_f32_e64 v32, v32 clamp
	v_exp_f32_e64 v33, v33 clamp
	v_exp_f32_e32 v44, v46
	v_exp_f32_e32 v45, v47
	v_pk_fma_f32 v[58:59], v[80:81], s[2:3], 1.0 op_sel_hi:[1,0,0]
	v_pk_fma_f32 v[60:61], v[82:83], s[2:3], 1.0 op_sel_hi:[1,0,0]
	v_pk_fma_f32 v[52:53], v[52:53], s[2:3], 1.0 op_sel_hi:[1,0,0]
	v_pk_fma_f32 v[22:23], v[22:23], s[2:3], 1.0 op_sel_hi:[1,0,0]
	v_pk_fma_f32 v[54:55], v[54:55], s[2:3], 1.0 op_sel_hi:[1,0,0]
	v_pk_fma_f32 v[56:57], v[56:57], s[2:3], 1.0 op_sel_hi:[1,0,0]
	v_pk_fma_f32 v[30:31], v[30:31], s[2:3], 1.0 op_sel_hi:[1,0,0]
	v_pk_fma_f32 v[32:33], v[32:33], s[2:3], 1.0 op_sel_hi:[1,0,0]
	v_pk_fma_f32 v[46:47], v[78:79], v[58:59], v[58:59]
	v_pk_fma_f32 v[48:49], v[48:49], v[60:61], v[60:61]
	v_pk_fma_f32 v[50:51], v[50:51], v[52:53], v[52:53]
	v_pk_fma_f32 v[20:21], v[20:21], v[22:23], v[22:23]
	v_pk_fma_f32 v[24:25], v[24:25], v[54:55], v[54:55]
	v_pk_fma_f32 v[34:35], v[34:35], v[56:57], v[56:57]
	v_pk_fma_f32 v[26:27], v[26:27], v[30:31], v[30:31]
	v_pk_fma_f32 v[28:29], v[28:29], v[32:33], v[32:33]
	v_pk_fma_f32 v[58:59], v[58:59], s[6:7], v[40:41] op_sel_hi:[1,0,0] neg_lo:[1,0,0] neg_hi:[1,0,0]
	v_pk_fma_f32 v[60:61], v[60:61], s[6:7], v[40:41] op_sel_hi:[1,0,0] neg_lo:[1,0,0] neg_hi:[1,0,0]
	v_pk_fma_f32 v[52:53], v[52:53], s[6:7], v[40:41] op_sel_hi:[1,0,0] neg_lo:[1,0,0] neg_hi:[1,0,0]
	v_pk_fma_f32 v[22:23], v[22:23], s[6:7], v[40:41] op_sel_hi:[1,0,0] neg_lo:[1,0,0] neg_hi:[1,0,0]
	v_pk_fma_f32 v[54:55], v[54:55], s[6:7], v[40:41] op_sel_hi:[1,0,0] neg_lo:[1,0,0] neg_hi:[1,0,0]
	v_pk_fma_f32 v[56:57], v[56:57], s[6:7], v[40:41] op_sel_hi:[1,0,0] neg_lo:[1,0,0] neg_hi:[1,0,0]
	v_pk_fma_f32 v[30:31], v[30:31], s[6:7], v[40:41] op_sel_hi:[1,0,0] neg_lo:[1,0,0] neg_hi:[1,0,0]
	v_pk_fma_f32 v[32:33], v[32:33], s[6:7], v[40:41] op_sel_hi:[1,0,0] neg_lo:[1,0,0] neg_hi:[1,0,0]
	v_pk_fma_f32 v[46:47], v[4:5], v[46:47], v[46:47]
	v_pk_fma_f32 v[48:49], v[6:7], v[48:49], v[48:49]
	v_pk_fma_f32 v[50:51], v[8:9], v[50:51], v[50:51]
	v_pk_fma_f32 v[20:21], v[10:11], v[20:21], v[20:21]
	v_pk_fma_f32 v[24:25], v[12:13], v[24:25], v[24:25]
	v_pk_fma_f32 v[34:35], v[18:19], v[34:35], v[34:35]
	v_pk_fma_f32 v[26:27], v[36:37], v[26:27], v[26:27]
	v_pk_fma_f32 v[28:29], v[44:45], v[28:29], v[28:29]
	v_rcp_f32_e64 v46, v46 clamp
	v_rcp_f32_e64 v47, v47 clamp
	v_rcp_f32_e64 v48, v48 clamp
	v_rcp_f32_e64 v49, v49 clamp
	v_rcp_f32_e64 v50, v50 clamp
	v_rcp_f32_e64 v51, v51 clamp
	v_rcp_f32_e64 v20, v20 clamp
	v_rcp_f32_e64 v21, v21 clamp
	v_rcp_f32_e64 v24, v24 clamp
	v_rcp_f32_e64 v25, v25 clamp
	v_rcp_f32_e64 v34, v34 clamp
	v_rcp_f32_e64 v35, v35 clamp
	v_rcp_f32_e64 v26, v26 clamp
	v_rcp_f32_e64 v27, v27 clamp
	v_rcp_f32_e64 v28, v28 clamp
	v_rcp_f32_e64 v29, v29 clamp
	v_pk_mul_f32 v[46:47], v[58:59], v[46:47]
	v_pk_mul_f32 v[48:49], v[60:61], v[48:49]
	v_pk_mul_f32 v[50:51], v[52:53], v[50:51]
	v_pk_mul_f32 v[20:21], v[22:23], v[20:21]
	v_pk_mul_f32 v[22:23], v[54:55], v[24:25]
	v_pk_mul_f32 v[24:25], v[56:57], v[34:35]
	v_pk_mul_f32 v[26:27], v[30:31], v[26:27]
	v_pk_mul_f32 v[28:29], v[32:33], v[28:29]
	v_pk_fma_f32 v[4:5], v[4:5], v[46:47], v[46:47]
	v_pk_fma_f32 v[6:7], v[6:7], v[48:49], v[48:49]
	v_pk_fma_f32 v[8:9], v[8:9], v[50:51], v[50:51]
	v_pk_fma_f32 v[10:11], v[10:11], v[20:21], v[20:21]
	v_pk_fma_f32 v[12:13], v[12:13], v[22:23], v[22:23]
	v_pk_fma_f32 v[18:19], v[18:19], v[24:25], v[24:25]
	v_pk_fma_f32 v[30:31], v[36:37], v[26:27], v[26:27]
	v_pk_fma_f32 v[32:33], v[44:45], v[28:29], v[28:29]
	s_nop 0
	v_pk_fma_f32 v[4:5], v[4:5], v[4:5], s[4:5] neg_lo:[1,0,0] neg_hi:[1,0,0] clamp
	v_pk_fma_f32 v[6:7], v[6:7], v[6:7], s[4:5] neg_lo:[1,0,0] neg_hi:[1,0,0] clamp
	v_pk_fma_f32 v[8:9], v[8:9], v[8:9], s[4:5] neg_lo:[1,0,0] neg_hi:[1,0,0] clamp
	v_pk_fma_f32 v[10:11], v[10:11], v[10:11], s[4:5] neg_lo:[1,0,0] neg_hi:[1,0,0] clamp
	v_pk_fma_f32 v[12:13], v[12:13], v[12:13], s[4:5] neg_lo:[1,0,0] neg_hi:[1,0,0] clamp
	v_pk_fma_f32 v[18:19], v[18:19], v[18:19], s[4:5] neg_lo:[1,0,0] neg_hi:[1,0,0] clamp
	v_pk_fma_f32 v[30:31], v[30:31], v[30:31], s[4:5] neg_lo:[1,0,0] neg_hi:[1,0,0] clamp
	s_nop 0
	v_pk_fma_f32 v[32:33], v[32:33], v[32:33], s[4:5] neg_lo:[1,0,0] neg_hi:[1,0,0] clamp
	s_nop 0
	v_pk_fma_f32 v[8:9], v[8:9], v[8:9], s[8:9] op_sel_hi:[1,1,0]
	v_pk_fma_f32 v[10:11], v[10:11], v[10:11], s[8:9] op_sel_hi:[1,1,0]
	v_pk_fma_f32 v[12:13], v[12:13], v[12:13], s[8:9] op_sel_hi:[1,1,0]
	v_pk_fma_f32 v[18:19], v[18:19], v[18:19], s[8:9] op_sel_hi:[1,1,0]
	v_pk_fma_f32 v[32:33], v[32:33], v[32:33], s[8:9] op_sel_hi:[1,1,0]
	v_pk_fma_f32 v[4:5], v[4:5], v[4:5], s[8:9] op_sel_hi:[1,1,0]
	v_pk_fma_f32 v[6:7], v[6:7], v[6:7], s[8:9] op_sel_hi:[1,1,0]
	v_pk_fma_f32 v[30:31], v[30:31], v[30:31], s[8:9] op_sel_hi:[1,1,0]
	v_pk_mul_f32 v[8:9], v[50:51], v[8:9]
	v_pk_mul_f32 v[84:85], v[20:21], v[10:11]
	v_pk_mul_f32 v[86:87], v[22:23], v[12:13]
	v_pk_mul_f32 v[10:11], v[24:25], v[18:19]
	v_pk_mul_f32 v[12:13], v[28:29], v[32:33]
	v_pk_mul_f32 v[64:65], v[46:47], v[4:5]
	v_pk_mul_f32 v[82:83], v[48:49], v[6:7]
	v_pk_mul_f32 v[20:21], v[30:31], v[26:27]
	ds_read_b128 v[4:7], v72 offset:6144
	ds_read_b128 v[22:25], v71 offset:42368
	ds_read_b128 v[26:29], v72 offset:7168
	ds_read_b128 v[30:33], v71 offset:42432
	v_cvt_pk_f16_f32 v19, v84, v85
	v_cvt_pk_f16_f32 v18, v8, v9
	v_cvt_pk_f16_f32 v20, v20, v21
	s_waitcnt lgkmcnt(2)
	v_mfma_f32_16x16x32_f16 v[34:37], v[4:7], v[14:17], v[22:25]
	v_cvt_pk_f16_f32 v21, v12, v13
	v_mfma_f32_16x16x32_f16 v[44:47], v[4:7], v[0:3], v[22:25]
	ds_read_b128 v[4:7], v72 offset:8192
	ds_read_b128 v[48:51], v71 offset:42496
	s_waitcnt lgkmcnt(2)
	v_cvt_pk_f16_f32 v22, v64, v65
	v_mfma_f32_16x16x32_f16 v[52:55], v[26:29], v[14:17], v[30:33]
	v_cvt_pk_f16_f32 v23, v82, v83
	v_cvt_pk_f16_f32 v24, v86, v87
	v_mfma_f32_16x16x32_f16 v[26:29], v[26:29], v[0:3], v[30:33]
	ds_read_b128 v[56:59], v71 offset:42560
	v_exp_f32_e32 v86, v34
	v_exp_f32_e32 v87, v35
	ds_read_b128 v[30:33], v72 offset:9216
	s_waitcnt lgkmcnt(2)
	v_mfma_f32_16x16x32_f16 v[60:63], v[4:7], v[14:17], v[48:51]
	v_exp_f32_e64 v88, v52 clamp
	v_exp_f32_e64 v89, v53 clamp
	v_exp_f32_e64 v90, v54 clamp
	v_mfma_f32_16x16x32_f16 v[48:51], v[4:7], v[0:3], v[48:51]
	ds_read_b128 v[64:67], v72 offset:10240
	ds_read_b128 v[74:77], v71 offset:42624
	s_nop 1
	v_exp_f32_e32 v4, v60
	s_waitcnt lgkmcnt(2)
	v_mfma_f32_16x16x32_f16 v[78:81], v[30:33], v[14:17], v[56:59]
	v_exp_f32_e32 v5, v61
	v_exp_f32_e32 v60, v36
	v_exp_f32_e32 v61, v37
	v_mfma_f32_16x16x32_f16 v[30:33], v[30:33], v[0:3], v[56:59]
	ds_read_b128 v[82:85], v71 offset:42688
	v_exp_f32_e64 v91, v55 clamp
	v_exp_f32_e32 v6, v62
	ds_read_b128 v[56:59], v72 offset:11264
	s_waitcnt lgkmcnt(2)
	v_mfma_f32_16x16x32_f16 v[34:37], v[64:67], v[14:17], v[74:77]
	v_exp_f32_e32 v7, v63
	v_exp_f32_e32 v8, v48
	v_exp_f32_e32 v9, v49
	v_mfma_f32_16x16x32_f16 v[52:55], v[64:67], v[0:3], v[74:77]
	v_exp_f32_e32 v44, v44
	v_exp_f32_e32 v45, v45
	v_exp_f32_e64 v26, v26 clamp
	s_waitcnt lgkmcnt(0)
	v_mfma_f32_16x16x32_f16 v[14:17], v[56:59], v[14:17], v[82:85]
	v_exp_f32_e64 v27, v27 clamp
	v_exp_f32_e32 v46, v46
	v_exp_f32_e32 v47, v47
	v_mfma_f32_16x16x32_f16 v[56:59], v[56:59], v[0:3], v[82:85]
	v_exp_f32_e64 v28, v28 clamp
	s_nop 2
	v_exp_f32_e32 v2, v14
	v_exp_f32_e32 v3, v15
	v_exp_f32_e32 v14, v16
	v_exp_f32_e32 v15, v17
	v_exp_f32_e32 v16, v30
	v_exp_f32_e32 v17, v31
	v_exp_f32_e64 v29, v29 clamp
	v_exp_f32_e32 v0, v50
	v_exp_f32_e32 v1, v51
	v_exp_f32_e32 v48, v78
	v_exp_f32_e32 v49, v79
	v_exp_f32_e64 v34, v34 clamp
	v_exp_f32_e64 v35, v35 clamp
	v_exp_f32_e32 v50, v80
	v_exp_f32_e32 v51, v81
	v_exp_f32_e64 v36, v36 clamp
	v_exp_f32_e64 v37, v37 clamp
	v_exp_f32_e64 v30, v52 clamp
	v_exp_f32_e64 v31, v53 clamp
	v_exp_f32_e32 v52, v56
	v_exp_f32_e32 v53, v57
	v_exp_f32_e32 v32, v32
	v_exp_f32_e32 v33, v33
	v_exp_f32_e64 v54, v54 clamp
	v_exp_f32_e64 v55, v55 clamp
	v_exp_f32_e32 v56, v58
	v_cvt_pk_f16_f32 v25, v10, v11
	v_exp_f32_e32 v57, v59
	v_pk_fma_f32 v[30:31], v[30:31], s[2:3], 1.0 op_sel_hi:[1,0,0]
	v_pk_fma_f32 v[10:11], v[88:89], s[2:3], 1.0 op_sel_hi:[1,0,0]
	v_pk_fma_f32 v[12:13], v[90:91], s[2:3], 1.0 op_sel_hi:[1,0,0]
	v_pk_fma_f32 v[26:27], v[26:27], s[2:3], 1.0 op_sel_hi:[1,0,0]
	v_pk_fma_f32 v[28:29], v[28:29], s[2:3], 1.0 op_sel_hi:[1,0,0]
	v_pk_fma_f32 v[34:35], v[34:35], s[2:3], 1.0 op_sel_hi:[1,0,0]
	v_pk_fma_f32 v[36:37], v[36:37], s[2:3], 1.0 op_sel_hi:[1,0,0]
	v_pk_fma_f32 v[54:55], v[54:55], s[2:3], 1.0 op_sel_hi:[1,0,0]
	v_pk_fma_f32 v[16:17], v[16:17], v[30:31], v[30:31]
	v_pk_fma_f32 v[58:59], v[86:87], v[10:11], v[10:11]
	v_pk_fma_f32 v[10:11], v[10:11], s[6:7], v[40:41] op_sel_hi:[1,0,0] neg_lo:[1,0,0] neg_hi:[1,0,0]
	v_pk_fma_f32 v[60:61], v[60:61], v[12:13], v[12:13]
	v_pk_fma_f32 v[12:13], v[12:13], s[6:7], v[40:41] op_sel_hi:[1,0,0] neg_lo:[1,0,0] neg_hi:[1,0,0]
	v_pk_fma_f32 v[44:45], v[44:45], v[26:27], v[26:27]
	v_pk_fma_f32 v[46:47], v[46:47], v[28:29], v[28:29]
	v_pk_fma_f32 v[48:49], v[48:49], v[34:35], v[34:35]
	v_pk_fma_f32 v[50:51], v[50:51], v[36:37], v[36:37]
	v_pk_fma_f32 v[32:33], v[32:33], v[54:55], v[54:55]
	v_pk_fma_f32 v[16:17], v[52:53], v[16:17], v[16:17]
	v_pk_fma_f32 v[26:27], v[26:27], s[6:7], v[40:41] op_sel_hi:[1,0,0] neg_lo:[1,0,0] neg_hi:[1,0,0]
	v_pk_fma_f32 v[28:29], v[28:29], s[6:7], v[40:41] op_sel_hi:[1,0,0] neg_lo:[1,0,0] neg_hi:[1,0,0]
	v_pk_fma_f32 v[34:35], v[34:35], s[6:7], v[40:41] op_sel_hi:[1,0,0] neg_lo:[1,0,0] neg_hi:[1,0,0]
	v_pk_fma_f32 v[36:37], v[36:37], s[6:7], v[40:41] op_sel_hi:[1,0,0] neg_lo:[1,0,0] neg_hi:[1,0,0]
	v_pk_fma_f32 v[30:31], v[30:31], s[6:7], v[40:41] op_sel_hi:[1,0,0] neg_lo:[1,0,0] neg_hi:[1,0,0]
	v_pk_fma_f32 v[54:55], v[54:55], s[6:7], v[40:41] op_sel_hi:[1,0,0] neg_lo:[1,0,0] neg_hi:[1,0,0]
	v_pk_fma_f32 v[58:59], v[4:5], v[58:59], v[58:59]
	v_pk_fma_f32 v[60:61], v[6:7], v[60:61], v[60:61]
	v_pk_fma_f32 v[44:45], v[8:9], v[44:45], v[44:45]
	v_pk_fma_f32 v[46:47], v[0:1], v[46:47], v[46:47]
	v_pk_fma_f32 v[48:49], v[2:3], v[48:49], v[48:49]
	v_pk_fma_f32 v[50:51], v[14:15], v[50:51], v[50:51]
	v_pk_fma_f32 v[32:33], v[56:57], v[32:33], v[32:33]
	v_rcp_f32_e64 v16, v16 clamp
	v_rcp_f32_e64 v17, v17 clamp
	v_rcp_f32_e64 v58, v58 clamp
	v_rcp_f32_e64 v59, v59 clamp
	v_rcp_f32_e64 v60, v60 clamp
	v_rcp_f32_e64 v61, v61 clamp
	v_rcp_f32_e64 v44, v44 clamp
	v_rcp_f32_e64 v45, v45 clamp
	v_rcp_f32_e64 v46, v46 clamp
	v_rcp_f32_e64 v47, v47 clamp
	v_rcp_f32_e64 v48, v48 clamp
	v_rcp_f32_e64 v49, v49 clamp
	v_rcp_f32_e64 v50, v50 clamp
	v_rcp_f32_e64 v51, v51 clamp
	v_rcp_f32_e64 v32, v32 clamp
	v_rcp_f32_e64 v33, v33 clamp
	v_pk_mul_f32 v[10:11], v[10:11], v[58:59]
	v_pk_mul_f32 v[12:13], v[12:13], v[60:61]
	v_pk_mul_f32 v[26:27], v[26:27], v[44:45]
	v_pk_mul_f32 v[34:35], v[34:35], v[48:49]
	v_pk_mul_f32 v[36:37], v[36:37], v[50:51]
	v_pk_mul_f32 v[28:29], v[28:29], v[46:47]
	v_pk_mul_f32 v[16:17], v[30:31], v[16:17]
	v_pk_mul_f32 v[30:31], v[54:55], v[32:33]
	v_pk_fma_f32 v[4:5], v[4:5], v[10:11], v[10:11]
	v_pk_fma_f32 v[6:7], v[6:7], v[12:13], v[12:13]
	v_pk_fma_f32 v[8:9], v[8:9], v[26:27], v[26:27]
	v_pk_fma_f32 v[2:3], v[2:3], v[34:35], v[34:35]
	v_pk_fma_f32 v[14:15], v[14:15], v[36:37], v[36:37]
	v_pk_fma_f32 v[0:1], v[0:1], v[28:29], v[28:29]
	v_pk_fma_f32 v[32:33], v[52:53], v[16:17], v[16:17]
	v_pk_fma_f32 v[44:45], v[56:57], v[30:31], v[30:31]
	s_nop 0
	v_pk_fma_f32 v[4:5], v[4:5], v[4:5], s[4:5] neg_lo:[1,0,0] neg_hi:[1,0,0] clamp
	v_pk_fma_f32 v[6:7], v[6:7], v[6:7], s[4:5] neg_lo:[1,0,0] neg_hi:[1,0,0] clamp
	v_pk_fma_f32 v[8:9], v[8:9], v[8:9], s[4:5] neg_lo:[1,0,0] neg_hi:[1,0,0] clamp
	v_pk_fma_f32 v[0:1], v[0:1], v[0:1], s[4:5] neg_lo:[1,0,0] neg_hi:[1,0,0] clamp
	v_pk_fma_f32 v[2:3], v[2:3], v[2:3], s[4:5] neg_lo:[1,0,0] neg_hi:[1,0,0] clamp
	v_pk_fma_f32 v[14:15], v[14:15], v[14:15], s[4:5] neg_lo:[1,0,0] neg_hi:[1,0,0] clamp
	v_pk_fma_f32 v[32:33], v[32:33], v[32:33], s[4:5] neg_lo:[1,0,0] neg_hi:[1,0,0] clamp
	s_nop 0
	v_pk_fma_f32 v[44:45], v[44:45], v[44:45], s[4:5] neg_lo:[1,0,0] neg_hi:[1,0,0] clamp
	s_nop 0
	v_pk_fma_f32 v[32:33], v[32:33], v[32:33], s[8:9] op_sel_hi:[1,1,0]
	v_pk_fma_f32 v[4:5], v[4:5], v[4:5], s[8:9] op_sel_hi:[1,1,0]
	v_pk_fma_f32 v[6:7], v[6:7], v[6:7], s[8:9] op_sel_hi:[1,1,0]
	v_pk_fma_f32 v[8:9], v[8:9], v[8:9], s[8:9] op_sel_hi:[1,1,0]
	v_pk_fma_f32 v[0:1], v[0:1], v[0:1], s[8:9] op_sel_hi:[1,1,0]
	v_pk_fma_f32 v[2:3], v[2:3], v[2:3], s[8:9] op_sel_hi:[1,1,0]
	v_pk_fma_f32 v[14:15], v[14:15], v[14:15], s[8:9] op_sel_hi:[1,1,0]
	v_pk_fma_f32 v[44:45], v[44:45], v[44:45], s[8:9] op_sel_hi:[1,1,0]
	v_pk_mul_f32 v[16:17], v[32:33], v[16:17]
	v_pk_mul_f32 v[52:53], v[10:11], v[4:5]
	v_pk_mul_f32 v[54:55], v[12:13], v[6:7]
	v_pk_mul_f32 v[26:27], v[26:27], v[8:9]
	v_pk_mul_f32 v[28:29], v[28:29], v[0:1]
	v_pk_mul_f32 v[56:57], v[34:35], v[2:3]
	v_pk_mul_f32 v[58:59], v[36:37], v[14:15]
	v_pk_mul_f32 v[60:61], v[30:31], v[44:45]
	s_cmp_lt_u32 s33, 8
	s_cbranch_scc1 .Lprio_half
	s_setprio 0
.Lprio_half:
	ds_read_b128 v[0:3], v72 offset:12288
	ds_read_b128 v[4:7], v71 offset:42752
	ds_read_b128 v[8:11], v72 offset:13312
	ds_read_b128 v[12:15], v72 offset:14336
	ds_read_b128 v[34:37], v72 offset:15360
	ds_read_b128 v[44:47], v71 offset:42816
	v_cvt_pk_f16_f32 v30, v52, v53
	v_cvt_pk_f16_f32 v26, v26, v27
	v_cvt_pk_f16_f32 v31, v54, v55
	s_waitcnt lgkmcnt(4)
	v_mfma_f32_16x16x32_f16 v[48:51], v[0:3], v[22:25], v[4:7]
	v_cvt_pk_f16_f32 v32, v56, v57
	v_cvt_pk_f16_f32 v33, v58, v59
	v_cvt_pk_f16_f32 v27, v28, v29
	v_mfma_f32_16x16x32_f16 v[0:3], v[0:3], v[18:21], v[4:7]
	v_cvt_pk_f16_f32 v28, v16, v17
	v_cvt_pk_f16_f32 v29, v60, v61
	s_add_i32 s11, s9, s12
	s_waitcnt lgkmcnt(3)
	v_mfma_f32_16x16x32_f16 v[48:51], v[8:11], v[30:33], v[48:51]
	s_cmp_lt_i32 s11, 0x8000
	s_cselect_b32 s10, s11, s10
	s_ashr_i32 s11, s10, 31
	v_mfma_f32_16x16x32_f16 v[52:55], v[8:11], v[26:29], v[0:3]
	ds_read_b128 v[4:7], v72 offset:17408
	ds_read_b128 v[8:11], v71 offset:42880
	s_lshl_b64 s[10:11], s[10:11], 12
	s_add_u32 s10, s10, s36
	s_addc_u32 s11, s11, s37
	ds_read_b128 v[0:3], v72 offset:16384
	s_waitcnt lgkmcnt(3)
	v_exp_f32_e32 v106, v48
	v_mfma_f32_16x16x32_f16 v[56:59], v[12:15], v[22:25], v[44:47]
	v_exp_f32_e32 v107, v49
	v_exp_f32_e32 v110, v50
	v_mfma_f32_16x16x32_f16 v[12:15], v[12:15], v[18:21], v[44:47]
	v_exp_f32_e32 v111, v51
	v_exp_f32_e32 v114, v52
	v_mfma_f32_16x16x32_f16 v[44:47], v[34:37], v[30:33], v[56:59]
	v_exp_f32_e32 v115, v53
	v_mfma_f32_16x16x32_f16 v[56:59], v[34:37], v[26:29], v[12:15]
	ds_read_b128 v[34:37], v72 offset:19456
	ds_read_b128 v[60:63], v71 offset:42944
	s_nop 4
	v_exp_f32_e64 v108, v44 clamp
	ds_read_b128 v[12:15], v72 offset:18432
	s_waitcnt lgkmcnt(3)
	v_mfma_f32_16x16x32_f16 v[64:67], v[0:3], v[22:25], v[8:11]
	v_exp_f32_e64 v109, v45 clamp
	v_exp_f32_e64 v112, v46 clamp
	v_mfma_f32_16x16x32_f16 v[0:3], v[0:3], v[18:21], v[8:11]
	v_exp_f32_e64 v116, v56 clamp
	v_mfma_f32_16x16x32_f16 v[64:67], v[4:7], v[30:33], v[64:67]
	v_exp_f32_e64 v59, v59 clamp
	v_mfma_f32_16x16x32_f16 v[74:77], v[4:7], v[26:29], v[0:3]
	ds_read_b128 v[78:81], v72 offset:20480
	ds_read_b128 v[82:85], v72 offset:21504
	ds_read_b128 v[86:89], v71 offset:43008
	s_waitcnt lgkmcnt(3)
	v_exp_f32_e64 v58, v58 clamp
	v_mfma_f32_16x16x32_f16 v[6:9], v[12:15], v[22:25], v[60:63]
	v_exp_f32_e64 v117, v57 clamp
	v_mfma_f32_16x16x32_f16 v[60:63], v[12:15], v[18:21], v[60:63]
	global_load_dwordx4 v[10:13], v39, s[10:11] offset:16
	global_load_dwordx4 v[14:17], v39, s[10:11]
	global_load_dwordx4 v[2:5], v39, s[10:11] offset:2064
	v_exp_f32_e64 v113, v47 clamp
	v_mfma_f32_16x16x32_f16 v[90:93], v[34:37], v[30:33], v[6:9]
	v_mfma_f32_16x16x32_f16 v[60:63], v[34:37], v[26:29], v[60:63]
	s_nop 1
	global_load_dwordx4 v[6:9], v39, s[10:11] offset:2048
	ds_read_b128 v[94:97], v72 offset:22528
	ds_read_b128 v[98:101], v72 offset:23552
	ds_read_b128 v[102:105], v71 offset:43072
	s_waitcnt lgkmcnt(3)
	v_exp_f32_e32 v0, v64
	v_mfma_f32_16x16x32_f16 v[44:47], v[78:81], v[22:25], v[86:89]
	v_exp_f32_e32 v1, v65
	v_exp_f32_e32 v34, v66
	v_mfma_f32_16x16x32_f16 v[48:51], v[78:81], v[18:21], v[86:89]
	v_exp_f32_e32 v35, v67
	v_exp_f32_e32 v36, v74
	v_exp_f32_e32 v37, v75
	v_mfma_f32_16x16x32_f16 v[64:67], v[82:85], v[30:33], v[44:47]
	v_exp_f32_e32 v74, v54
	v_exp_f32_e32 v75, v55
	v_exp_f32_e32 v78, v92
	v_mfma_f32_16x16x32_f16 v[50:53], v[82:85], v[26:29], v[48:51]
	v_exp_f32_e32 v44, v76
	v_exp_f32_e32 v45, v77
	v_exp_f32_e32 v76, v90
	s_waitcnt lgkmcnt(0)
	v_mfma_f32_16x16x32_f16 v[46:49], v[94:97], v[22:25], v[102:105]
	v_exp_f32_e32 v77, v91
	v_exp_f32_e64 v64, v64 clamp
	v_exp_f32_e64 v65, v65 clamp
	v_mfma_f32_16x16x32_f16 v[54:57], v[94:97], v[18:21], v[102:105]
	v_exp_f32_e32 v79, v93
	v_exp_f32_e64 v66, v66 clamp
	v_exp_f32_e64 v67, v67 clamp
	v_mfma_f32_16x16x32_f16 v[46:49], v[98:101], v[30:33], v[46:49]
	v_exp_f32_e32 v60, v60
	v_exp_f32_e32 v61, v61
	v_exp_f32_e64 v50, v50 clamp
	v_mfma_f32_16x16x32_f16 v[54:57], v[98:101], v[26:29], v[54:57]
	v_exp_f32_e64 v51, v51 clamp
	s_nop 2
	v_exp_f32_e32 v46, v46
	v_exp_f32_e32 v47, v47
	v_exp_f32_e32 v48, v48
	v_exp_f32_e32 v49, v49
	v_exp_f32_e32 v54, v54
	v_exp_f32_e32 v55, v55
	v_exp_f32_e32 v62, v62
	v_exp_f32_e32 v63, v63
	v_exp_f32_e64 v52, v52 clamp
	v_exp_f32_e64 v53, v53 clamp
	v_exp_f32_e32 v56, v56
	v_exp_f32_e32 v57, v57
	v_pk_fma_f32 v[80:81], v[108:109], s[2:3], 1.0 op_sel_hi:[1,0,0]
	v_pk_fma_f32 v[82:83], v[112:113], s[2:3], 1.0 op_sel_hi:[1,0,0]
	v_pk_fma_f32 v[84:85], v[116:117], s[2:3], 1.0 op_sel_hi:[1,0,0]
	v_pk_fma_f32 v[58:59], v[58:59], s[2:3], 1.0 op_sel_hi:[1,0,0]
	v_pk_fma_f32 v[64:65], v[64:65], s[2:3], 1.0 op_sel_hi:[1,0,0]
	v_pk_fma_f32 v[66:67], v[66:67], s[2:3], 1.0 op_sel_hi:[1,0,0]
	v_pk_fma_f32 v[50:51], v[50:51], s[2:3], 1.0 op_sel_hi:[1,0,0]
	v_pk_fma_f32 v[52:53], v[52:53], s[2:3], 1.0 op_sel_hi:[1,0,0]
	v_pk_fma_f32 v[86:87], v[106:107], v[80:81], v[80:81]
	v_pk_fma_f32 v[88:89], v[110:111], v[82:83], v[82:83]
	v_pk_fma_f32 v[90:91], v[114:115], v[84:85], v[84:85]
	v_pk_fma_f32 v[74:75], v[74:75], v[58:59], v[58:59]
	v_pk_fma_f32 v[76:77], v[76:77], v[64:65], v[64:65]
	v_pk_fma_f32 v[78:79], v[78:79], v[66:67], v[66:67]
	v_pk_fma_f32 v[60:61], v[60:61], v[50:51], v[50:51]
	v_pk_fma_f32 v[62:63], v[62:63], v[52:53], v[52:53]
	v_pk_fma_f32 v[80:81], v[80:81], s[6:7], v[40:41] op_sel_hi:[1,0,0] neg_lo:[1,0,0] neg_hi:[1,0,0]
	v_pk_fma_f32 v[82:83], v[82:83], s[6:7], v[40:41] op_sel_hi:[1,0,0] neg_lo:[1,0,0] neg_hi:[1,0,0]
	v_pk_fma_f32 v[84:85], v[84:85], s[6:7], v[40:41] op_sel_hi:[1,0,0] neg_lo:[1,0,0] neg_hi:[1,0,0]
	v_pk_fma_f32 v[58:59], v[58:59], s[6:7], v[40:41] op_sel_hi:[1,0,0] neg_lo:[1,0,0] neg_hi:[1,0,0]
	v_pk_fma_f32 v[64:65], v[64:65], s[6:7], v[40:41] op_sel_hi:[1,0,0] neg_lo:[1,0,0] neg_hi:[1,0,0]
	v_pk_fma_f32 v[66:67], v[66:67], s[6:7], v[40:41] op_sel_hi:[1,0,0] neg_lo:[1,0,0] neg_hi:[1,0,0]
	v_pk_fma_f32 v[50:51], v[50:51], s[6:7], v[40:41] op_sel_hi:[1,0,0] neg_lo:[1,0,0] neg_hi:[1,0,0]
	v_pk_fma_f32 v[52:53], v[52:53], s[6:7], v[40:41] op_sel_hi:[1,0,0] neg_lo:[1,0,0] neg_hi:[1,0,0]
	v_pk_fma_f32 v[86:87], v[0:1], v[86:87], v[86:87]
	v_pk_fma_f32 v[88:89], v[34:35], v[88:89], v[88:89]
	v_pk_fma_f32 v[90:91], v[36:37], v[90:91], v[90:91]
	v_pk_fma_f32 v[74:75], v[44:45], v[74:75], v[74:75]
	v_pk_fma_f32 v[76:77], v[46:47], v[76:77], v[76:77]
	v_pk_fma_f32 v[78:79], v[48:49], v[78:79], v[78:79]
	v_pk_fma_f32 v[60:61], v[54:55], v[60:61], v[60:61]
	v_pk_fma_f32 v[62:63], v[56:57], v[62:63], v[62:63]
	v_rcp_f32_e64 v86, v86 clamp
	v_rcp_f32_e64 v87, v87 clamp
	v_rcp_f32_e64 v88, v88 clamp
	v_rcp_f32_e64 v89, v89 clamp
	v_rcp_f32_e64 v90, v90 clamp
	v_rcp_f32_e64 v91, v91 clamp
	v_rcp_f32_e64 v74, v74 clamp
	v_rcp_f32_e64 v75, v75 clamp
	v_rcp_f32_e64 v76, v76 clamp
	v_rcp_f32_e64 v77, v77 clamp
	v_rcp_f32_e64 v78, v78 clamp
	v_rcp_f32_e64 v79, v79 clamp
	v_rcp_f32_e64 v60, v60 clamp
	v_rcp_f32_e64 v61, v61 clamp
	v_rcp_f32_e64 v62, v62 clamp
	v_rcp_f32_e64 v63, v63 clamp
	v_pk_mul_f32 v[80:81], v[80:81], v[86:87]
	v_pk_mul_f32 v[82:83], v[82:83], v[88:89]
	v_pk_mul_f32 v[84:85], v[84:85], v[90:91]
	v_pk_mul_f32 v[58:59], v[58:59], v[74:75]
	v_pk_mul_f32 v[64:65], v[64:65], v[76:77]
	v_pk_mul_f32 v[66:67], v[66:67], v[78:79]
	v_pk_mul_f32 v[50:51], v[50:51], v[60:61]
	v_pk_mul_f32 v[60:61], v[52:53], v[62:63]
	v_pk_fma_f32 v[0:1], v[0:1], v[80:81], v[80:81]
	v_pk_fma_f32 v[34:35], v[34:35], v[82:83], v[82:83]
	v_pk_fma_f32 v[36:37], v[36:37], v[84:85], v[84:85]
	v_pk_fma_f32 v[44:45], v[44:45], v[58:59], v[58:59]
	v_pk_fma_f32 v[46:47], v[46:47], v[64:65], v[64:65]
	v_pk_fma_f32 v[48:49], v[48:49], v[66:67], v[66:67]
	v_pk_fma_f32 v[52:53], v[54:55], v[50:51], v[50:51]
	v_pk_fma_f32 v[54:55], v[56:57], v[60:61], v[60:61]
	s_nop 0
	v_pk_fma_f32 v[0:1], v[0:1], v[0:1], s[4:5] neg_lo:[1,0,0] neg_hi:[1,0,0] clamp
	v_pk_fma_f32 v[34:35], v[34:35], v[34:35], s[4:5] neg_lo:[1,0,0] neg_hi:[1,0,0] clamp
	v_pk_fma_f32 v[36:37], v[36:37], v[36:37], s[4:5] neg_lo:[1,0,0] neg_hi:[1,0,0] clamp
	v_pk_fma_f32 v[44:45], v[44:45], v[44:45], s[4:5] neg_lo:[1,0,0] neg_hi:[1,0,0] clamp
	v_pk_fma_f32 v[46:47], v[46:47], v[46:47], s[4:5] neg_lo:[1,0,0] neg_hi:[1,0,0] clamp
	v_pk_fma_f32 v[48:49], v[48:49], v[48:49], s[4:5] neg_lo:[1,0,0] neg_hi:[1,0,0] clamp
	v_pk_fma_f32 v[52:53], v[52:53], v[52:53], s[4:5] neg_lo:[1,0,0] neg_hi:[1,0,0] clamp
	s_nop 0
	v_pk_fma_f32 v[54:55], v[54:55], v[54:55], s[4:5] neg_lo:[1,0,0] neg_hi:[1,0,0] clamp
	s_nop 0
	v_pk_fma_f32 v[0:1], v[0:1], v[0:1], s[8:9] op_sel_hi:[1,1,0]
	v_pk_fma_f32 v[56:57], v[34:35], v[34:35], s[8:9] op_sel_hi:[1,1,0]
	v_pk_fma_f32 v[36:37], v[36:37], v[36:37], s[8:9] op_sel_hi:[1,1,0]
	v_pk_fma_f32 v[44:45], v[44:45], v[44:45], s[8:9] op_sel_hi:[1,1,0]
	v_pk_fma_f32 v[46:47], v[46:47], v[46:47], s[8:9] op_sel_hi:[1,1,0]
	v_pk_fma_f32 v[48:49], v[48:49], v[48:49], s[8:9] op_sel_hi:[1,1,0]
	v_pk_fma_f32 v[62:63], v[52:53], v[52:53], s[8:9] op_sel_hi:[1,1,0]
	v_pk_fma_f32 v[74:75], v[54:55], v[54:55], s[8:9] op_sel_hi:[1,1,0]
	v_pk_mul_f32 v[34:35], v[80:81], v[0:1]
	v_pk_mul_f32 v[56:57], v[82:83], v[56:57]
	v_pk_mul_f32 v[36:37], v[84:85], v[36:37]
	v_pk_mul_f32 v[52:53], v[58:59], v[44:45]
	v_pk_mul_f32 v[54:55], v[64:65], v[46:47]
	v_pk_mul_f32 v[0:1], v[66:67], v[48:49]
	v_pk_mul_f32 v[46:47], v[62:63], v[50:51]
	v_pk_mul_f32 v[44:45], v[60:61], v[74:75]
	ds_read_b128 v[48:51], v72 offset:24576
	ds_read_b128 v[58:61], v71 offset:43136
	ds_read_b128 v[62:65], v72 offset:25600
	ds_read_b128 v[74:77], v72 offset:26624
	ds_read_b128 v[78:81], v72 offset:27648
	ds_read_b128 v[82:85], v71 offset:43200
	v_cvt_pk_f16_f32 v34, v34, v35
	s_waitcnt lgkmcnt(4)
	v_mfma_f32_16x16x32_f16 v[86:89], v[48:51], v[22:25], v[58:61]
	v_cvt_pk_f16_f32 v35, v56, v57
	v_mfma_f32_16x16x32_f16 v[48:51], v[48:51], v[18:21], v[58:61]
	s_waitcnt lgkmcnt(3)
	v_mfma_f32_16x16x32_f16 v[58:61], v[62:65], v[30:33], v[86:89]
	v_mfma_f32_16x16x32_f16 v[86:89], v[62:65], v[26:29], v[48:51]
	ds_read_b128 v[62:65], v72 offset:29696
	ds_read_b128 v[90:93], v71 offset:43264
	s_nop 2
	ds_read_b128 v[48:51], v72 offset:28672
	s_waitcnt lgkmcnt(3)
	v_mfma_f32_16x16x32_f16 v[94:97], v[74:77], v[22:25], v[82:85]
	v_exp_f32_e32 v120, v86
	v_mfma_f32_16x16x32_f16 v[74:77], v[74:77], v[18:21], v[82:85]
	v_exp_f32_e32 v123, v89
	v_mfma_f32_16x16x32_f16 v[82:85], v[78:81], v[30:33], v[94:97]
	v_exp_f32_e32 v122, v88
	v_mfma_f32_16x16x32_f16 v[74:77], v[78:81], v[26:29], v[74:77]
	ds_read_b128 v[78:81], v72 offset:30720
	s_nop 0
	ds_read_b128 v[94:97], v72 offset:31744
	ds_read_b128 v[98:101], v71 offset:43328
	s_waitcnt lgkmcnt(3)
	v_exp_f32_e32 v121, v87
	v_mfma_f32_16x16x32_f16 v[102:105], v[48:51], v[22:25], v[90:93]
	s_nop 0
	v_exp_f32_e64 v66, v82 clamp
	v_exp_f32_e64 v67, v83 clamp
	v_exp_f32_e64 v118, v84 clamp
	v_mfma_f32_16x16x32_f16 v[48:51], v[48:51], v[18:21], v[90:93]
	v_exp_f32_e64 v119, v85 clamp
	v_exp_f32_e64 v124, v74 clamp
	v_exp_f32_e64 v125, v75 clamp
	v_mfma_f32_16x16x32_f16 v[90:93], v[62:65], v[30:33], v[102:105]
	v_exp_f32_e64 v126, v76 clamp
	v_exp_f32_e64 v127, v77 clamp
	v_mfma_f32_16x16x32_f16 v[102:105], v[62:65], v[26:29], v[48:51]
	ds_read_b128 v[106:109], v72 offset:32768
	ds_read_b128 v[110:113], v72 offset:33792
	v_exp_f32_e32 v62, v58
	v_exp_f32_e32 v63, v59
	v_exp_f32_e32 v64, v60
	v_exp_f32_e32 v65, v61
	ds_read_b128 v[114:117], v71 offset:43392
	s_waitcnt lgkmcnt(3)
	v_mfma_f32_16x16x32_f16 v[58:61], v[78:81], v[22:25], v[98:101]
	v_exp_f32_e32 v48, v90
	v_exp_f32_e32 v49, v91
	v_mfma_f32_16x16x32_f16 v[78:81], v[78:81], v[18:21], v[98:101]
	v_exp_f32_e32 v51, v93
	v_mfma_f32_16x16x32_f16 v[82:85], v[94:97], v[30:33], v[58:61]
	v_exp_f32_e32 v50, v92
	v_mfma_f32_16x16x32_f16 v[78:81], v[94:97], v[26:29], v[78:81]
	ds_read_b128 v[86:89], v72 offset:34816
	ds_read_b128 v[90:93], v72 offset:35840
	ds_read_b128 v[94:97], v71 offset:43456
	s_waitcnt lgkmcnt(3)
	v_exp_f32_e32 v58, v102
	v_mfma_f32_16x16x32_f16 v[74:77], v[106:109], v[22:25], v[114:117]
	v_exp_f32_e32 v59, v103
	v_exp_f32_e32 v60, v104
	v_mfma_f32_16x16x32_f16 v[98:101], v[106:109], v[18:21], v[114:117]
	v_exp_f32_e32 v61, v105
	v_exp_f32_e32 v102, v82
	v_exp_f32_e32 v103, v83
	v_exp_f32_e32 v104, v84
	v_mfma_f32_16x16x32_f16 v[74:77], v[110:113], v[30:33], v[74:77]
	v_exp_f32_e32 v105, v85
	v_mfma_f32_16x16x32_f16 v[82:85], v[110:113], v[26:29], v[98:101]
	s_waitcnt lgkmcnt(0)
	v_mfma_f32_16x16x32_f16 v[18:21], v[86:89], v[18:21], v[94:97]
	s_nop 4
	v_exp_f32_e64 v106, v74 clamp
	v_exp_f32_e64 v107, v75 clamp
	v_exp_f32_e64 v108, v76 clamp
	v_exp_f32_e64 v109, v77 clamp
	v_mfma_f32_16x16x32_f16 v[74:77], v[86:89], v[22:25], v[94:97]
	v_cvt_pk_f16_f32 v22, v36, v37
	v_cvt_pk_f16_f32 v23, v52, v53
	v_cvt_pk_f16_f32 v36, v54, v55
	v_mfma_f32_16x16x32_f16 v[18:21], v[90:93], v[26:29], v[18:21]
	v_exp_f32_e32 v52, v78
	v_exp_f32_e32 v53, v79
	v_exp_f32_e64 v54, v82 clamp
	v_mfma_f32_16x16x32_f16 v[30:33], v[90:93], v[30:33], v[74:77]
	v_exp_f32_e64 v55, v83 clamp
	s_nop 2
	v_exp_f32_e32 v18, v18
	v_exp_f32_e32 v19, v19
	v_exp_f32_e32 v26, v80
	v_exp_f32_e32 v27, v81
	v_exp_f32_e32 v30, v30
	v_exp_f32_e32 v31, v31
	v_exp_f32_e32 v32, v32
	v_exp_f32_e32 v33, v33
	v_exp_f32_e64 v28, v84 clamp
	v_exp_f32_e64 v29, v85 clamp
	v_exp_f32_e32 v20, v20
	v_cvt_pk_f16_f32 v24, v46, v47
	v_cvt_pk_f16_f32 v37, v0, v1
	v_cvt_pk_f16_f32 v25, v44, v45
	v_exp_f32_e32 v21, v21
	v_pk_fma_f32 v[0:1], v[66:67], s[2:3], 1.0 op_sel_hi:[1,0,0]
	v_pk_fma_f32 v[44:45], v[118:119], s[2:3], 1.0 op_sel_hi:[1,0,0]
	v_pk_fma_f32 v[46:47], v[124:125], s[2:3], 1.0 op_sel_hi:[1,0,0]
	v_pk_fma_f32 v[56:57], v[126:127], s[2:3], 1.0 op_sel_hi:[1,0,0]
	v_pk_fma_f32 v[66:67], v[106:107], s[2:3], 1.0 op_sel_hi:[1,0,0]
	v_pk_fma_f32 v[74:75], v[108:109], s[2:3], 1.0 op_sel_hi:[1,0,0]
	v_pk_fma_f32 v[54:55], v[54:55], s[2:3], 1.0 op_sel_hi:[1,0,0]
	v_pk_fma_f32 v[28:29], v[28:29], s[2:3], 1.0 op_sel_hi:[1,0,0]
	v_pk_fma_f32 v[62:63], v[62:63], v[0:1], v[0:1]
	v_pk_fma_f32 v[64:65], v[64:65], v[44:45], v[44:45]
	v_pk_fma_f32 v[76:77], v[120:121], v[46:47], v[46:47]
	v_pk_fma_f32 v[78:79], v[122:123], v[56:57], v[56:57]
	v_pk_fma_f32 v[80:81], v[102:103], v[66:67], v[66:67]
	v_pk_fma_f32 v[82:83], v[104:105], v[74:75], v[74:75]
	v_pk_fma_f32 v[52:53], v[52:53], v[54:55], v[54:55]
	v_pk_fma_f32 v[26:27], v[26:27], v[28:29], v[28:29]
	v_pk_fma_f32 v[0:1], v[0:1], s[6:7], v[40:41] op_sel_hi:[1,0,0] neg_lo:[1,0,0] neg_hi:[1,0,0]
	v_pk_fma_f32 v[44:45], v[44:45], s[6:7], v[40:41] op_sel_hi:[1,0,0] neg_lo:[1,0,0] neg_hi:[1,0,0]
	v_pk_fma_f32 v[46:47], v[46:47], s[6:7], v[40:41] op_sel_hi:[1,0,0] neg_lo:[1,0,0] neg_hi:[1,0,0]
	v_pk_fma_f32 v[56:57], v[56:57], s[6:7], v[40:41] op_sel_hi:[1,0,0] neg_lo:[1,0,0] neg_hi:[1,0,0]
	v_pk_fma_f32 v[66:67], v[66:67], s[6:7], v[40:41] op_sel_hi:[1,0,0] neg_lo:[1,0,0] neg_hi:[1,0,0]
	v_pk_fma_f32 v[74:75], v[74:75], s[6:7], v[40:41] op_sel_hi:[1,0,0] neg_lo:[1,0,0] neg_hi:[1,0,0]
	v_pk_fma_f32 v[54:55], v[54:55], s[6:7], v[40:41] op_sel_hi:[1,0,0] neg_lo:[1,0,0] neg_hi:[1,0,0]
	v_pk_fma_f32 v[28:29], v[28:29], s[6:7], v[40:41] op_sel_hi:[1,0,0] neg_lo:[1,0,0] neg_hi:[1,0,0]
	v_pk_fma_f32 v[62:63], v[48:49], v[62:63], v[62:63]
	v_pk_fma_f32 v[64:65], v[50:51], v[64:65], v[64:65]
	v_pk_fma_f32 v[76:77], v[58:59], v[76:77], v[76:77]
	v_pk_fma_f32 v[78:79], v[60:61], v[78:79], v[78:79]
	v_pk_fma_f32 v[80:81], v[30:31], v[80:81], v[80:81]
	v_pk_fma_f32 v[82:83], v[32:33], v[82:83], v[82:83]
	v_pk_fma_f32 v[52:53], v[18:19], v[52:53], v[52:53]
	v_pk_fma_f32 v[26:27], v[20:21], v[26:27], v[26:27]
	v_rcp_f32_e64 v62, v62 clamp
	v_rcp_f32_e64 v63, v63 clamp
	v_rcp_f32_e64 v64, v64 clamp
	v_rcp_f32_e64 v65, v65 clamp
	v_rcp_f32_e64 v76, v76 clamp
	v_rcp_f32_e64 v77, v77 clamp
	v_rcp_f32_e64 v78, v78 clamp
	v_rcp_f32_e64 v79, v79 clamp
	v_rcp_f32_e64 v80, v80 clamp
	v_rcp_f32_e64 v81, v81 clamp
	v_rcp_f32_e64 v82, v82 clamp
	v_rcp_f32_e64 v83, v83 clamp
	v_rcp_f32_e64 v52, v52 clamp
	v_rcp_f32_e64 v53, v53 clamp
	v_rcp_f32_e64 v26, v26 clamp
	v_rcp_f32_e64 v27, v27 clamp
	v_pk_mul_f32 v[52:53], v[54:55], v[52:53]
	v_pk_mul_f32 v[0:1], v[0:1], v[62:63]
	v_pk_mul_f32 v[44:45], v[44:45], v[64:65]
	v_pk_mul_f32 v[46:47], v[46:47], v[76:77]
	v_pk_mul_f32 v[56:57], v[56:57], v[78:79]
	v_pk_mul_f32 v[62:63], v[66:67], v[80:81]
	v_pk_mul_f32 v[64:65], v[74:75], v[82:83]
	v_pk_mul_f32 v[26:27], v[28:29], v[26:27]
	v_pk_fma_f32 v[18:19], v[18:19], v[52:53], v[52:53]
	v_pk_fma_f32 v[28:29], v[48:49], v[0:1], v[0:1]
	v_pk_fma_f32 v[48:49], v[50:51], v[44:45], v[44:45]
	v_pk_fma_f32 v[50:51], v[58:59], v[46:47], v[46:47]
	v_pk_fma_f32 v[54:55], v[60:61], v[56:57], v[56:57]
	v_pk_fma_f32 v[30:31], v[30:31], v[62:63], v[62:63]
	v_pk_fma_f32 v[32:33], v[32:33], v[64:65], v[64:65]
	v_pk_fma_f32 v[20:21], v[20:21], v[26:27], v[26:27]
	s_nop 0
	v_pk_fma_f32 v[28:29], v[28:29], v[28:29], s[4:5] neg_lo:[1,0,0] neg_hi:[1,0,0] clamp
	v_pk_fma_f32 v[48:49], v[48:49], v[48:49], s[4:5] neg_lo:[1,0,0] neg_hi:[1,0,0] clamp
	v_pk_fma_f32 v[50:51], v[50:51], v[50:51], s[4:5] neg_lo:[1,0,0] neg_hi:[1,0,0] clamp
	v_pk_fma_f32 v[54:55], v[54:55], v[54:55], s[4:5] neg_lo:[1,0,0] neg_hi:[1,0,0] clamp
	v_pk_fma_f32 v[30:31], v[30:31], v[30:31], s[4:5] neg_lo:[1,0,0] neg_hi:[1,0,0] clamp
	v_pk_fma_f32 v[32:33], v[32:33], v[32:33], s[4:5] neg_lo:[1,0,0] neg_hi:[1,0,0] clamp
	v_pk_fma_f32 v[18:19], v[18:19], v[18:19], s[4:5] neg_lo:[1,0,0] neg_hi:[1,0,0] clamp
	s_nop 0
	v_pk_fma_f32 v[20:21], v[20:21], v[20:21], s[4:5] neg_lo:[1,0,0] neg_hi:[1,0,0] clamp
	s_nop 0
	v_pk_fma_f32 v[28:29], v[28:29], v[28:29], s[8:9] op_sel_hi:[1,1,0]
	v_pk_fma_f32 v[48:49], v[48:49], v[48:49], s[8:9] op_sel_hi:[1,1,0]
	v_pk_fma_f32 v[50:51], v[50:51], v[50:51], s[8:9] op_sel_hi:[1,1,0]
	v_pk_fma_f32 v[54:55], v[54:55], v[54:55], s[8:9] op_sel_hi:[1,1,0]
	v_pk_fma_f32 v[30:31], v[30:31], v[30:31], s[8:9] op_sel_hi:[1,1,0]
	v_pk_fma_f32 v[32:33], v[32:33], v[32:33], s[8:9] op_sel_hi:[1,1,0]
	v_pk_fma_f32 v[18:19], v[18:19], v[18:19], s[8:9] op_sel_hi:[1,1,0]
	v_pk_fma_f32 v[20:21], v[20:21], v[20:21], s[8:9] op_sel_hi:[1,1,0]
	v_pk_mul_f32 v[0:1], v[0:1], v[28:29]
	v_pk_mul_f32 v[58:59], v[44:45], v[48:49]
	v_pk_mul_f32 v[60:61], v[46:47], v[50:51]
	v_pk_mul_f32 v[54:55], v[56:57], v[54:55]
	v_pk_mul_f32 v[62:63], v[62:63], v[30:31]
	v_pk_mul_f32 v[64:65], v[64:65], v[32:33]
	v_pk_mul_f32 v[66:67], v[18:19], v[52:53]
	v_pk_mul_f32 v[74:75], v[26:27], v[20:21]
	ds_read_b128 v[18:21], v72 offset:36864
	ds_read_b128 v[30:33], v72 offset:37888
	ds_read_b128 v[26:29], v71 offset:43520
	v_cvt_pk_f16_f32 v56, v60, v61
	v_cvt_pk_f16_f32 v57, v54, v55
	v_cvt_pk_f16_f32 v54, v62, v63
	ds_read_b128 v[60:63], v71 offset:43584
	v_cvt_pk_f16_f32 v52, v0, v1
	v_cvt_pk_f16_f32 v53, v58, v59
	s_waitcnt lgkmcnt(1)
	v_mfma_f32_16x16x32_f16 v[48:51], v[18:21], v[34:37], v[26:29]
	v_cvt_pk_f16_f32 v55, v64, v65
	v_cvt_pk_f16_f32 v58, v66, v67
	v_mfma_f32_16x16x32_f16 v[18:21], v[18:21], v[22:25], v[26:29]
	ds_read_b128 v[44:47], v72 offset:40960
	s_add_i32 s12, s12, s3
	s_add_i32 s10, s20, s12
	v_cvt_pk_f16_f32 v59, v74, v75
	v_mfma_f32_16x16x32_f16 v[26:29], v[30:33], v[52:55], v[48:51]
	s_cmp_lt_i32 s10, 0x8000
	v_add_u32_e32 v38, s7, v38
	s_nop 0
	ds_read_b128 v[48:51], v72 offset:38912
	v_mfma_f32_16x16x32_f16 v[18:21], v[30:33], v[56:59], v[18:21]
	ds_read_b128 v[30:33], v72 offset:39936
	s_nop 1
	v_cvt_pk_f16_f32 v1, v28, v29
	v_cvt_pk_f16_f32 v0, v26, v27
	s_waitcnt lgkmcnt(1)
	v_mfma_f32_16x16x32_f16 v[34:37], v[48:51], v[34:37], v[60:63]
	v_pk_max_f16 v27, v1, 0
	v_cvt_pk_f16_f32 v1, v20, v21
	v_pk_max_f16 v26, v0, 0
	v_mfma_f32_16x16x32_f16 v[20:23], v[48:51], v[22:25], v[60:63]
	v_cvt_pk_f16_f32 v0, v18, v19
	v_pk_max_f16 v18, v0, 0
	s_waitcnt lgkmcnt(0)
	v_mfma_f32_16x16x32_f16 v[34:37], v[30:33], v[52:55], v[34:37]
	v_pk_max_f16 v19, v1, 0
	v_mfma_f32_16x16x32_f16 v[20:23], v[30:33], v[56:59], v[20:23]
	s_nop 6
	v_cvt_pk_f16_f32 v0, v34, v35
	v_cvt_pk_f16_f32 v1, v36, v37
	v_pk_max_f16 v28, v0, 0
	v_pk_max_f16 v29, v1, 0
	v_cvt_pk_f16_f32 v0, v20, v21
	v_cvt_pk_f16_f32 v1, v22, v23
	v_pk_max_f16 v20, v0, 0
	v_pk_max_f16 v21, v1, 0
	v_mfma_f32_16x16x32_f16 v[24:27], v[44:47], v[26:29], 0
	s_nop 0
	v_mfma_f32_16x16x32_f16 v[18:21], v[44:47], v[18:21], 0
	s_nop 7
	v_cndmask_b32_e64 v18, v24, v18, s[0:1]
	s_cbranch_scc0 .LBB0_37
